# P7 side job carried in the SP2 MFMA block (partner issues 2 stage DMAs there) instead of the SP1 block (partner issues 6); SP1 block pure; half tiles run the job alone
# baseline (speedup 1.0000x reference)
.Lp7vg_wd_a1:
	s_waitcnt lgkmcnt(0)
	s_barrier
	s_setprio 1
	v_mfma_scale_f32_16x16x128_f8f6f4 v[202:205], v[26:33], v[58:65], v[202:205], v226, v226 op_sel_hi:[0,0,0]
	s_add_u32 s2, s42, 0xfffc0080
	s_addc_u32 s3, s43, -1
	s_cmp_eq_u32 s64, 12
	s_cselect_b32 s5, s23, s3
	s_cselect_b32 s4, s25, s2
	s_cselect_b32 s45, s35, s63
	s_cselect_b32 s44, s61, s62
	v_mfma_scale_f32_16x16x128_f8f6f4 v[198:201], v[18:25], v[58:65], v[198:201], v226, v226 op_sel_hi:[0,0,0]
	v_mfma_scale_f32_16x16x128_f8f6f4 v[186:189], v[26:33], v[50:57], v[186:189], v226, v226 op_sel_hi:[0,0,0]
	v_mfma_scale_f32_16x16x128_f8f6f4 v[182:185], v[18:25], v[50:57], v[182:185], v226, v226 op_sel_hi:[0,0,0]
	v_mfma_scale_f32_16x16x128_f8f6f4 v[170:173], v[26:33], v[42:49], v[170:173], v226, v226 op_sel_hi:[0,0,0]
	v_mfma_scale_f32_16x16x128_f8f6f4 v[166:169], v[18:25], v[42:49], v[166:169], v226, v226 op_sel_hi:[0,0,0]
	v_mfma_scale_f32_16x16x128_f8f6f4 v[154:157], v[26:33], v[34:41], v[154:157], v226, v226 op_sel_hi:[0,0,0]
	v_mfma_scale_f32_16x16x128_f8f6f4 v[150:153], v[18:25], v[34:41], v[150:153], v226, v226 op_sel_hi:[0,0,0]
	s_setprio 0
	s_setprio 1
	v_mfma_scale_f32_16x16x128_f8f6f4 v[194:197], v[10:17], v[58:65], v[194:197], v226, v226 op_sel_hi:[0,0,0]
	v_mfma_scale_f32_16x16x128_f8f6f4 v[190:193], v[2:9], v[58:65], v[190:193], v226, v226 op_sel_hi:[0,0,0]
	v_mfma_scale_f32_16x16x128_f8f6f4 v[178:181], v[10:17], v[50:57], v[178:181], v226, v226 op_sel_hi:[0,0,0]
	v_mfma_scale_f32_16x16x128_f8f6f4 v[174:177], v[2:9], v[50:57], v[174:177], v226, v226 op_sel_hi:[0,0,0]
	v_mfma_scale_f32_16x16x128_f8f6f4 v[162:165], v[10:17], v[42:49], v[162:165], v226, v226 op_sel_hi:[0,0,0]
	v_mfma_scale_f32_16x16x128_f8f6f4 v[158:161], v[2:9], v[42:49], v[158:161], v226, v226 op_sel_hi:[0,0,0]
	v_mfma_scale_f32_16x16x128_f8f6f4 v[146:149], v[10:17], v[34:41], v[146:149], v226, v226 op_sel_hi:[0,0,0]
	v_mfma_scale_f32_16x16x128_f8f6f4 v[142:145], v[2:9], v[34:41], v[142:145], v226, v226 op_sel_hi:[0,0,0]
	s_setprio 0

; #define PG8_LAS __attribute__((address_space(3)))
;     __device__ __forceinline__ void issue(PG8_LAS unsigned char* lds0, int j, int tid, int wid) const {
;         const float* s0; unsigned char* d; addr(j, tid, s0, d);
;         __builtin_amdgcn_global_load_lds((const unsigned*)s0, (PG8_LAS unsigned*)(lds0 + stage + wid * 1024), 16, 0, 2);
;         __builtin_amdgcn_global_load_lds((const unsigned*)(s0 + ntot), (PG8_LAS unsigned*)(lds0 + stage + 8192 + wid * 1024), 16, 0, 2);
;     }
;     __device__ __forceinline__ void read(v4i_t& t0, v4i_t& t1, int tid, unsigned ldsb) const {
;         asm volatile("ds_read_b128 %0, %1" : "=&v"(t0) : "v"(ldsb + stage + 16u * (unsigned)tid) : "memory");
;         asm volatile("ds_read_b128 %0, %1" : "=&v"(t1) : "v"(ldsb + stage + 8192u + 16u * (unsigned)tid) : "memory");
;     }
;     __device__ __forceinline__ void finish(v4i_t& t0, v4i_t& t1, int j, int tid) const {
;         asm volatile("" : "+v"(t0), "+v"(t1));
;         const float* s0; unsigned char* d; addr(j, tid, s0, d);
;         const f32x4 r0 = __builtin_bit_cast(f32x4, t0) * 64.f, r1 = __builtin_bit_cast(f32x4, t1) * 64.f;
;         int w0 = 0, w1 = 0; w0 = __builtin_amdgcn_cvt_pk_fp8_f32(r0[0], r1[0], w0, false); w0 = __builtin_amdgcn_cvt_pk_fp8_f32(r0[1], r1[1], w0, true);
;         w1 = __builtin_amdgcn_cvt_pk_fp8_f32(r0[2], r1[2], w1, false); w1 = __builtin_amdgcn_cvt_pk_fp8_f32(r0[3], r1[3], w1, true);
;         typedef int v2is __attribute__((ext_vector_type(2))); __builtin_nontemporal_store((v2is){w0, w1}, (v2is*)d);
.Lp7dma_wd_a:
	s_waitcnt lgkmcnt(0)
	s_barrier
	s_cbranch_vccnz .Lp7dma_skip_b
	s_cmp_lt_i32 s98, 0
	s_cbranch_scc1 .Lp7m2_slow_a
	s_cmpk_gt_i32 s48, 0x7f
	s_cbranch_scc1 .Lp7m2_slow_a
	s_setprio 1
	v_mfma_scale_f32_16x16x128_f8f6f4 v[138:141], v[26:33], v[58:65], v[138:141], v226, v226 op_sel_hi:[0,0,0]
	s_add_i32 s68, s98, s52
	s_add_i32 s68, s68, 1
	v_mul_f32_e32 v70, s14, v70
	v_mfma_scale_f32_16x16x128_f8f6f4 v[134:137], v[18:25], v[58:65], v[134:137], v226, v226 op_sel_hi:[0,0,0]
	v_mul_f32_e32 v74, s14, v74
	v_mul_f32_e32 v71, s14, v71
	v_mul_f32_e32 v75, s14, v75
	v_mfma_scale_f32_16x16x128_f8f6f4 v[122:125], v[26:33], v[50:57], v[122:125], v226, v226 op_sel_hi:[0,0,0]
	s_lshl_b32 s68, s68, 12
	v_cvt_pk_fp8_f32 v70, v70, v74
	v_mul_f32_e32 v72, s14, v72
	v_mfma_scale_f32_16x16x128_f8f6f4 v[118:121], v[18:25], v[50:57], v[118:121], v226, v226 op_sel_hi:[0,0,0]
	v_mul_f32_e32 v76, s14, v76
	v_cvt_pk_fp8_f32 v70, v71, v75 op_sel:[0,0,1]
	v_mul_f32_e32 v73, s14, v73
	v_mfma_scale_f32_16x16x128_f8f6f4 v[106:109], v[26:33], v[42:49], v[106:109], v226, v226 op_sel_hi:[0,0,0]
	v_mul_f32_e32 v77, s14, v77
	v_readlane_b32 s66, v251, 50
	v_cvt_pk_fp8_f32 v71, v72, v76
	v_mfma_scale_f32_16x16x128_f8f6f4 v[102:105], v[18:25], v[42:49], v[102:105], v226, v226 op_sel_hi:[0,0,0]
	v_readlane_b32 s67, v251, 51
	v_cvt_pk_fp8_f32 v71, v73, v77 op_sel:[0,0,1]
	s_add_u32 s66, s66, s68
	s_addc_u32 s67, s67, 0
	v_mfma_scale_f32_16x16x128_f8f6f4 v[90:93], v[26:33], v[34:41], v[90:93], v226, v226 op_sel_hi:[0,0,0]
	global_store_dwordx2 v210, v[70:71], s[66:67] nt
	s_add_i32 s68, s48, s53
	s_lshl_b32 s68, s68, 14
	v_mfma_scale_f32_16x16x128_f8f6f4 v[86:89], v[18:25], v[34:41], v[86:89], v226, v226 op_sel_hi:[0,0,0]
	s_setprio 0
	s_setprio 1
	s_add_u32 s66, s76, s68
	s_addc_u32 s67, s77, 0
	s_add_u32 s70, s66, s16
	s_addc_u32 s71, s67, s17
	v_mfma_scale_f32_16x16x128_f8f6f4 v[130:133], v[10:17], v[58:65], v[130:133], v226, v226 op_sel_hi:[0,0,0]
	v_lshlrev_b32_e32 v66, 2, v208
	global_load_dwordx4 v[70:73], v66, s[66:67] nt
	global_load_dwordx4 v[74:77], v66, s[70:71] nt
	v_mfma_scale_f32_16x16x128_f8f6f4 v[126:129], v[2:9], v[58:65], v[126:129], v226, v226 op_sel_hi:[0,0,0]
	s_mov_b32 s100, 3
	s_mov_b32 s98, s48
	s_add_i32 s48, s48, 1
	v_mfma_scale_f32_16x16x128_f8f6f4 v[114:117], v[10:17], v[50:57], v[114:117], v226, v226 op_sel_hi:[0,0,0]
	v_mfma_scale_f32_16x16x128_f8f6f4 v[110:113], v[2:9], v[50:57], v[110:113], v226, v226 op_sel_hi:[0,0,0]
	v_mfma_scale_f32_16x16x128_f8f6f4 v[98:101], v[10:17], v[42:49], v[98:101], v226, v226 op_sel_hi:[0,0,0]
	v_mfma_scale_f32_16x16x128_f8f6f4 v[94:97], v[2:9], v[42:49], v[94:97], v226, v226 op_sel_hi:[0,0,0]
	v_mfma_scale_f32_16x16x128_f8f6f4 v[82:85], v[10:17], v[34:41], v[82:85], v226, v226 op_sel_hi:[0,0,0]
	v_mfma_scale_f32_16x16x128_f8f6f4 v[78:81], v[2:9], v[34:41], v[78:81], v226, v226 op_sel_hi:[0,0,0]
	s_setprio 0

.Lp7vg_wd_b1:
	s_waitcnt lgkmcnt(0)
	s_barrier
	s_setprio 1
	v_mfma_scale_f32_16x16x128_f8f6f4 v[202:205], v[26:33], v[58:65], v[202:205], v226, v226 op_sel_hi:[0,0,0]
	s_add_u32 s46, s44, 0x84000
	s_addc_u32 s47, s45, 0
	v_mfma_scale_f32_16x16x128_f8f6f4 v[198:201], v[18:25], v[58:65], v[198:201], v226, v226 op_sel_hi:[0,0,0]
	v_mfma_scale_f32_16x16x128_f8f6f4 v[186:189], v[26:33], v[50:57], v[186:189], v226, v226 op_sel_hi:[0,0,0]
	v_mfma_scale_f32_16x16x128_f8f6f4 v[182:185], v[18:25], v[50:57], v[182:185], v226, v226 op_sel_hi:[0,0,0]
	v_mfma_scale_f32_16x16x128_f8f6f4 v[170:173], v[26:33], v[42:49], v[170:173], v226, v226 op_sel_hi:[0,0,0]
	v_mfma_scale_f32_16x16x128_f8f6f4 v[166:169], v[18:25], v[42:49], v[166:169], v226, v226 op_sel_hi:[0,0,0]
	v_mfma_scale_f32_16x16x128_f8f6f4 v[154:157], v[26:33], v[34:41], v[154:157], v226, v226 op_sel_hi:[0,0,0]
	v_mfma_scale_f32_16x16x128_f8f6f4 v[150:153], v[18:25], v[34:41], v[150:153], v226, v226 op_sel_hi:[0,0,0]
	s_setprio 0
	s_setprio 1
	v_mfma_scale_f32_16x16x128_f8f6f4 v[194:197], v[10:17], v[58:65], v[194:197], v226, v226 op_sel_hi:[0,0,0]
	v_mfma_scale_f32_16x16x128_f8f6f4 v[190:193], v[2:9], v[58:65], v[190:193], v226, v226 op_sel_hi:[0,0,0]
	v_mfma_scale_f32_16x16x128_f8f6f4 v[178:181], v[10:17], v[50:57], v[178:181], v226, v226 op_sel_hi:[0,0,0]
	v_mfma_scale_f32_16x16x128_f8f6f4 v[174:177], v[2:9], v[50:57], v[174:177], v226, v226 op_sel_hi:[0,0,0]
	v_mfma_scale_f32_16x16x128_f8f6f4 v[162:165], v[10:17], v[42:49], v[162:165], v226, v226 op_sel_hi:[0,0,0]
	v_mfma_scale_f32_16x16x128_f8f6f4 v[158:161], v[2:9], v[42:49], v[158:161], v226, v226 op_sel_hi:[0,0,0]
	v_mfma_scale_f32_16x16x128_f8f6f4 v[146:149], v[10:17], v[34:41], v[146:149], v226, v226 op_sel_hi:[0,0,0]
	v_mfma_scale_f32_16x16x128_f8f6f4 v[142:145], v[2:9], v[34:41], v[142:145], v226, v226 op_sel_hi:[0,0,0]
	s_setprio 0

; #define PG8_LAS __attribute__((address_space(3)))
;     __device__ __forceinline__ void issue(PG8_LAS unsigned char* lds0, int j, int tid, int wid) const {
;         const float* s0; unsigned char* d; addr(j, tid, s0, d);
;         __builtin_amdgcn_global_load_lds((const unsigned*)s0, (PG8_LAS unsigned*)(lds0 + stage + wid * 1024), 16, 0, 2);
;         __builtin_amdgcn_global_load_lds((const unsigned*)(s0 + ntot), (PG8_LAS unsigned*)(lds0 + stage + 8192 + wid * 1024), 16, 0, 2);
;     }
;     __device__ __forceinline__ void read(v4i_t& t0, v4i_t& t1, int tid, unsigned ldsb) const {
;         asm volatile("ds_read_b128 %0, %1" : "=&v"(t0) : "v"(ldsb + stage + 16u * (unsigned)tid) : "memory");
;         asm volatile("ds_read_b128 %0, %1" : "=&v"(t1) : "v"(ldsb + stage + 8192u + 16u * (unsigned)tid) : "memory");
;     }
;     __device__ __forceinline__ void finish(v4i_t& t0, v4i_t& t1, int j, int tid) const {
;         asm volatile("" : "+v"(t0), "+v"(t1));
;         const float* s0; unsigned char* d; addr(j, tid, s0, d);
;         const f32x4 r0 = __builtin_bit_cast(f32x4, t0) * 64.f, r1 = __builtin_bit_cast(f32x4, t1) * 64.f;
;         int w0 = 0, w1 = 0; w0 = __builtin_amdgcn_cvt_pk_fp8_f32(r0[0], r1[0], w0, false); w0 = __builtin_amdgcn_cvt_pk_fp8_f32(r0[1], r1[1], w0, true);
;         w1 = __builtin_amdgcn_cvt_pk_fp8_f32(r0[2], r1[2], w1, false); w1 = __builtin_amdgcn_cvt_pk_fp8_f32(r0[3], r1[3], w1, true);
;         typedef int v2is __attribute__((ext_vector_type(2))); __builtin_nontemporal_store((v2is){w0, w1}, (v2is*)d);
.Lp7dma_wd_b:
	s_waitcnt lgkmcnt(0)
	s_barrier
	s_cbranch_vccnz .Lp7dma_skip_d
	s_cmp_lt_i32 s99, 0
	s_cbranch_scc1 .Lp7m2_slow_b
	s_cmpk_gt_i32 s48, 0x7f
	s_cbranch_scc1 .Lp7m2_slow_b
	s_setprio 1
	v_mfma_scale_f32_16x16x128_f8f6f4 v[138:141], v[26:33], v[58:65], v[138:141], v226, v226 op_sel_hi:[0,0,0]
	s_add_i32 s68, s99, s52
	s_add_i32 s68, s68, 1
	v_mul_f32_e32 v242, s14, v242
	v_mfma_scale_f32_16x16x128_f8f6f4 v[134:137], v[18:25], v[58:65], v[134:137], v226, v226 op_sel_hi:[0,0,0]
	v_mul_f32_e32 v246, s14, v246
	v_mul_f32_e32 v243, s14, v243
	v_mul_f32_e32 v247, s14, v247
	v_mfma_scale_f32_16x16x128_f8f6f4 v[122:125], v[26:33], v[50:57], v[122:125], v226, v226 op_sel_hi:[0,0,0]
	s_lshl_b32 s68, s68, 12
	v_cvt_pk_fp8_f32 v242, v242, v246
	v_mul_f32_e32 v244, s14, v244
	v_mfma_scale_f32_16x16x128_f8f6f4 v[118:121], v[18:25], v[50:57], v[118:121], v226, v226 op_sel_hi:[0,0,0]
	v_mul_f32_e32 v248, s14, v248
	v_cvt_pk_fp8_f32 v242, v243, v247 op_sel:[0,0,1]
	v_mul_f32_e32 v245, s14, v245
	v_mfma_scale_f32_16x16x128_f8f6f4 v[106:109], v[26:33], v[42:49], v[106:109], v226, v226 op_sel_hi:[0,0,0]
	v_mul_f32_e32 v249, s14, v249
	v_readlane_b32 s66, v251, 50
	v_cvt_pk_fp8_f32 v243, v244, v248
	v_mfma_scale_f32_16x16x128_f8f6f4 v[102:105], v[18:25], v[42:49], v[102:105], v226, v226 op_sel_hi:[0,0,0]
	v_readlane_b32 s67, v251, 51
	v_cvt_pk_fp8_f32 v243, v245, v249 op_sel:[0,0,1]
	s_add_u32 s66, s66, s68
	s_addc_u32 s67, s67, 0
	v_mfma_scale_f32_16x16x128_f8f6f4 v[90:93], v[26:33], v[34:41], v[90:93], v226, v226 op_sel_hi:[0,0,0]
	global_store_dwordx2 v210, v[242:243], s[66:67] nt
	s_add_i32 s68, s48, s53
	s_lshl_b32 s68, s68, 14
	v_mfma_scale_f32_16x16x128_f8f6f4 v[86:89], v[18:25], v[34:41], v[86:89], v226, v226 op_sel_hi:[0,0,0]
	s_setprio 0
	s_setprio 1
	s_add_u32 s66, s76, s68
	s_addc_u32 s67, s77, 0
	s_add_u32 s70, s66, s16
	s_addc_u32 s71, s67, s17
	v_mfma_scale_f32_16x16x128_f8f6f4 v[130:133], v[10:17], v[58:65], v[130:133], v226, v226 op_sel_hi:[0,0,0]
	v_lshlrev_b32_e32 v66, 2, v208
	global_load_dwordx4 v[242:245], v66, s[66:67] nt
	global_load_dwordx4 v[246:249], v66, s[70:71] nt
	v_mfma_scale_f32_16x16x128_f8f6f4 v[126:129], v[2:9], v[58:65], v[126:129], v226, v226 op_sel_hi:[0,0,0]
	s_mov_b32 s100, 3
	s_mov_b32 s99, s48
	s_add_i32 s48, s48, 1
	v_mfma_scale_f32_16x16x128_f8f6f4 v[114:117], v[10:17], v[50:57], v[114:117], v226, v226 op_sel_hi:[0,0,0]
	v_mfma_scale_f32_16x16x128_f8f6f4 v[110:113], v[2:9], v[50:57], v[110:113], v226, v226 op_sel_hi:[0,0,0]
	v_mfma_scale_f32_16x16x128_f8f6f4 v[98:101], v[10:17], v[42:49], v[98:101], v226, v226 op_sel_hi:[0,0,0]
	v_mfma_scale_f32_16x16x128_f8f6f4 v[94:97], v[2:9], v[42:49], v[94:97], v226, v226 op_sel_hi:[0,0,0]
	v_mfma_scale_f32_16x16x128_f8f6f4 v[82:85], v[10:17], v[34:41], v[82:85], v226, v226 op_sel_hi:[0,0,0]
	v_mfma_scale_f32_16x16x128_f8f6f4 v[78:81], v[2:9], v[34:41], v[78:81], v226, v226 op_sel_hi:[0,0,0]
	s_setprio 0
	s_branch .LBB0_781
.Lp7dma_skip_b:
	s_mov_b32 s100, 0
	s_cmp_lt_i32 s98, 0
	s_cbranch_scc1 .Lp7m2_nf_as
	s_add_i32 s68, s98, s52
	s_add_i32 s68, s68, 1
	v_mul_f32_e32 v70, s14, v70
	v_mul_f32_e32 v74, s14, v74
	v_mul_f32_e32 v71, s14, v71
	v_mul_f32_e32 v75, s14, v75
	s_lshl_b32 s68, s68, 12
	v_cvt_pk_fp8_f32 v70, v70, v74
	v_mul_f32_e32 v72, s14, v72
	v_mul_f32_e32 v76, s14, v76
	v_cvt_pk_fp8_f32 v70, v71, v75 op_sel:[0,0,1]
	v_mul_f32_e32 v73, s14, v73
	v_mul_f32_e32 v77, s14, v77
	v_readlane_b32 s66, v251, 50
	v_cvt_pk_fp8_f32 v71, v72, v76
	v_readlane_b32 s67, v251, 51
	v_cvt_pk_fp8_f32 v71, v73, v77 op_sel:[0,0,1]
	s_add_u32 s66, s66, s68
	s_addc_u32 s67, s67, 0
	global_store_dwordx2 v210, v[70:71], s[66:67] nt
	s_mov_b32 s100, 1
.Lp7m2_nf_as:
	s_mov_b32 s98, -1
	s_cmpk_gt_i32 s48, 0x7f
	s_cbranch_scc1 .Lp7m2_ni_as
	s_add_i32 s68, s48, s53
	s_lshl_b32 s68, s68, 14
	s_add_u32 s66, s76, s68
	s_addc_u32 s67, s77, 0
	s_add_u32 s70, s66, s16
	s_addc_u32 s71, s67, s17
	v_lshlrev_b32_e32 v66, 2, v208
	global_load_dwordx4 v[70:73], v66, s[66:67] nt
	global_load_dwordx4 v[74:77], v66, s[70:71] nt
	s_mov_b32 s98, s48
	s_add_i32 s48, s48, 1
	s_add_i32 s100, s100, 2

; #define PG8_LAS __attribute__((address_space(3)))
;     __device__ __forceinline__ void issue(PG8_LAS unsigned char* lds0, int j, int tid, int wid) const {
;         const float* s0; unsigned char* d; addr(j, tid, s0, d);
;         __builtin_amdgcn_global_load_lds((const unsigned*)s0, (PG8_LAS unsigned*)(lds0 + stage + wid * 1024), 16, 0, 2);
;         __builtin_amdgcn_global_load_lds((const unsigned*)(s0 + ntot), (PG8_LAS unsigned*)(lds0 + stage + 8192 + wid * 1024), 16, 0, 2);
;     }
;     __device__ __forceinline__ void read(v4i_t& t0, v4i_t& t1, int tid, unsigned ldsb) const {
;         asm volatile("ds_read_b128 %0, %1" : "=&v"(t0) : "v"(ldsb + stage + 16u * (unsigned)tid) : "memory");
;         asm volatile("ds_read_b128 %0, %1" : "=&v"(t1) : "v"(ldsb + stage + 8192u + 16u * (unsigned)tid) : "memory");
;     }
;     __device__ __forceinline__ void finish(v4i_t& t0, v4i_t& t1, int j, int tid) const {
;         asm volatile("" : "+v"(t0), "+v"(t1));
;         const float* s0; unsigned char* d; addr(j, tid, s0, d);
;         const f32x4 r0 = __builtin_bit_cast(f32x4, t0) * 64.f, r1 = __builtin_bit_cast(f32x4, t1) * 64.f;
;         int w0 = 0, w1 = 0; w0 = __builtin_amdgcn_cvt_pk_fp8_f32(r0[0], r1[0], w0, false); w0 = __builtin_amdgcn_cvt_pk_fp8_f32(r0[1], r1[1], w0, true);
;         w1 = __builtin_amdgcn_cvt_pk_fp8_f32(r0[2], r1[2], w1, false); w1 = __builtin_amdgcn_cvt_pk_fp8_f32(r0[3], r1[3], w1, true);
;         typedef int v2is __attribute__((ext_vector_type(2))); __builtin_nontemporal_store((v2is){w0, w1}, (v2is*)d);
.Lp7m2_ni_ag:
	s_setprio 1
	v_mfma_scale_f32_16x16x128_f8f6f4 v[138:141], v[26:33], v[58:65], v[138:141], v226, v226 op_sel_hi:[0,0,0]
	v_mfma_scale_f32_16x16x128_f8f6f4 v[134:137], v[18:25], v[58:65], v[134:137], v226, v226 op_sel_hi:[0,0,0]
	v_mfma_scale_f32_16x16x128_f8f6f4 v[122:125], v[26:33], v[50:57], v[122:125], v226, v226 op_sel_hi:[0,0,0]
	v_mfma_scale_f32_16x16x128_f8f6f4 v[118:121], v[18:25], v[50:57], v[118:121], v226, v226 op_sel_hi:[0,0,0]
	v_mfma_scale_f32_16x16x128_f8f6f4 v[106:109], v[26:33], v[42:49], v[106:109], v226, v226 op_sel_hi:[0,0,0]
	v_mfma_scale_f32_16x16x128_f8f6f4 v[102:105], v[18:25], v[42:49], v[102:105], v226, v226 op_sel_hi:[0,0,0]
	v_mfma_scale_f32_16x16x128_f8f6f4 v[90:93], v[26:33], v[34:41], v[90:93], v226, v226 op_sel_hi:[0,0,0]
	v_mfma_scale_f32_16x16x128_f8f6f4 v[86:89], v[18:25], v[34:41], v[86:89], v226, v226 op_sel_hi:[0,0,0]
	s_setprio 0
	s_setprio 1
	v_mfma_scale_f32_16x16x128_f8f6f4 v[130:133], v[10:17], v[58:65], v[130:133], v226, v226 op_sel_hi:[0,0,0]
	v_mfma_scale_f32_16x16x128_f8f6f4 v[126:129], v[2:9], v[58:65], v[126:129], v226, v226 op_sel_hi:[0,0,0]
	v_mfma_scale_f32_16x16x128_f8f6f4 v[114:117], v[10:17], v[50:57], v[114:117], v226, v226 op_sel_hi:[0,0,0]
	v_mfma_scale_f32_16x16x128_f8f6f4 v[110:113], v[2:9], v[50:57], v[110:113], v226, v226 op_sel_hi:[0,0,0]
	v_mfma_scale_f32_16x16x128_f8f6f4 v[98:101], v[10:17], v[42:49], v[98:101], v226, v226 op_sel_hi:[0,0,0]
	v_mfma_scale_f32_16x16x128_f8f6f4 v[94:97], v[2:9], v[42:49], v[94:97], v226, v226 op_sel_hi:[0,0,0]
	v_mfma_scale_f32_16x16x128_f8f6f4 v[82:85], v[10:17], v[34:41], v[82:85], v226, v226 op_sel_hi:[0,0,0]
	v_mfma_scale_f32_16x16x128_f8f6f4 v[78:81], v[2:9], v[34:41], v[78:81], v226, v226 op_sel_hi:[0,0,0]
	s_setprio 0
	s_branch .LBB0_790
.Lp7dma_skip_d:
	s_mov_b32 s100, 0
	s_cmp_lt_i32 s99, 0
	s_cbranch_scc1 .Lp7m2_nf_bs
	s_add_i32 s68, s99, s52
	s_add_i32 s68, s68, 1
	v_mul_f32_e32 v242, s14, v242
	v_mul_f32_e32 v246, s14, v246
	v_mul_f32_e32 v243, s14, v243
	v_mul_f32_e32 v247, s14, v247
	s_lshl_b32 s68, s68, 12
	v_cvt_pk_fp8_f32 v242, v242, v246
	v_mul_f32_e32 v244, s14, v244
	v_mul_f32_e32 v248, s14, v248
	v_cvt_pk_fp8_f32 v242, v243, v247 op_sel:[0,0,1]
	v_mul_f32_e32 v245, s14, v245
	v_mul_f32_e32 v249, s14, v249
	v_readlane_b32 s66, v251, 50
	v_cvt_pk_fp8_f32 v243, v244, v248
	v_readlane_b32 s67, v251, 51
	v_cvt_pk_fp8_f32 v243, v245, v249 op_sel:[0,0,1]
	s_add_u32 s66, s66, s68
	s_addc_u32 s67, s67, 0
	global_store_dwordx2 v210, v[242:243], s[66:67] nt
	s_mov_b32 s100, 1
.Lp7m2_nf_bs:
	s_mov_b32 s99, -1
	s_cmpk_gt_i32 s48, 0x7f
	s_cbranch_scc1 .Lp7m2_ni_bs
	s_add_i32 s68, s48, s53
	s_lshl_b32 s68, s68, 14
	s_add_u32 s66, s76, s68
	s_addc_u32 s67, s77, 0
	s_add_u32 s70, s66, s16
	s_addc_u32 s71, s67, s17
	v_lshlrev_b32_e32 v66, 2, v208
	global_load_dwordx4 v[242:245], v66, s[66:67] nt
	global_load_dwordx4 v[246:249], v66, s[70:71] nt
	s_mov_b32 s99, s48
	s_add_i32 s48, s48, 1
	s_add_i32 s100, s100, 2
